# grid barrier: L1 invalidate issued at arrival instead of after release; L1 rowpass hoists; gate-weight staging and p->bf16 loops with loads in flight
# speedup vs baseline: 1.0240x; 1.0240x over previous
; __device__ __forceinline__ unsigned pk2(float lo, float hi) { unsigned r; asm("v_cvt_pk_bf16_f32 %0, %1, %2" : "=v"(r) : "v"(lo), "v"(hi)); return r; }
; __device__ __forceinline__ void phase_p0a(const Ptrs& P, LAS unsigned char* lds, int tid_, int vcu, int G) {
;     ...
;     for (size_t i = gt; i < (size_t)NL * T * 256 / 8; i += NGT) { const f32x4 a = __builtin_nontemporal_load((const f32x4*)P.p + 2 * i), b = __builtin_nontemporal_load((const f32x4*)P.p + 2 * i + 1);
;         v4u w; w.x = pk2(a[0], a[1]); w.y = pk2(a[2], a[3]); w.z = pk2(b[0], b[1]); w.w = pk2(b[2], b[3]); ((v4u*)(P.ws + WS_PB))[i] = w; }
.LBB0_97:
	s_or_b64 exec, exec, s[8:9]
	s_mov_b64 s[4:5], 0x200000
	v_cmp_gt_u64_e64 s[4:5], s[4:5], v[2:3]
	s_and_saveexec_b64 s[8:9], s[4:5]
	s_cbranch_execz .LBB0_100
	s_lshl_b64 s[4:5], s[86:87], 13
	s_add_u32 s4, s0, s4
	s_addc_u32 s5, s1, s5
	v_lshl_add_u64 v[4:5], v[130:131], 4, s[4:5]
	s_mov_b64 s[4:5], 0x67a00000
	v_lshl_add_u64 v[4:5], v[4:5], 0, s[4:5]
	s_lshl_b64 s[10:11], s[68:69], 13
	s_lshl_b64 s[4:5], s[86:87], 14
	s_add_u32 s4, s28, s4
	s_waitcnt vmcnt(38)
	v_lshlrev_b64 v[6:7], 5, v[130:131]
	s_addc_u32 s5, s29, s5
	v_lshl_add_u64 v[6:7], s[4:5], 0, v[6:7]
	v_lshl_add_u64 v[6:7], v[6:7], 0, 16
	s_lshl_b64 s[12:13], s[68:69], 14
	s_mov_b64 s[14:15], 0
	s_mov_b64 s[16:17], 0x1fffff
	v_mov_b64_e32 v[8:9], v[2:3]
	s_cmpk_lg_i32 s68, 0x100
	s_cbranch_scc1 .LBB0_99
	s_mov_b32 s4, 4
.Lpcvt_loop:
	global_load_dwordx4 v[34:37], v[6:7], off offset:-16 nt
	global_load_dwordx4 v[38:41], v[6:7], off nt
	v_lshl_add_u64 v[6:7], v[6:7], 0, s[12:13]
	global_load_dwordx4 v[42:45], v[6:7], off offset:-16 nt
	global_load_dwordx4 v[46:49], v[6:7], off nt
	v_lshl_add_u64 v[6:7], v[6:7], 0, s[12:13]
	global_load_dwordx4 v[50:53], v[6:7], off offset:-16 nt
	global_load_dwordx4 v[54:57], v[6:7], off nt
	v_lshl_add_u64 v[6:7], v[6:7], 0, s[12:13]
	global_load_dwordx4 v[58:61], v[6:7], off offset:-16 nt
	global_load_dwordx4 v[62:65], v[6:7], off nt
	v_lshl_add_u64 v[6:7], v[6:7], 0, s[12:13]
	s_waitcnt vmcnt(6)
	v_cvt_pk_bf16_f32 v34, v34, v35
	v_cvt_pk_bf16_f32 v35, v36, v37
	v_cvt_pk_bf16_f32 v36, v38, v39
	v_cvt_pk_bf16_f32 v37, v40, v41
	global_store_dwordx4 v[4:5], v[34:37], off
	v_lshl_add_u64 v[4:5], v[4:5], 0, s[10:11]
	s_waitcnt vmcnt(5)
	v_cvt_pk_bf16_f32 v42, v42, v43
	v_cvt_pk_bf16_f32 v43, v44, v45
	v_cvt_pk_bf16_f32 v44, v46, v47
	v_cvt_pk_bf16_f32 v45, v48, v49
	global_store_dwordx4 v[4:5], v[42:45], off
	v_lshl_add_u64 v[4:5], v[4:5], 0, s[10:11]
	s_waitcnt vmcnt(4)
	v_cvt_pk_bf16_f32 v50, v50, v51
	v_cvt_pk_bf16_f32 v51, v52, v53
	v_cvt_pk_bf16_f32 v52, v54, v55
	v_cvt_pk_bf16_f32 v53, v56, v57
	global_store_dwordx4 v[4:5], v[50:53], off
	v_lshl_add_u64 v[4:5], v[4:5], 0, s[10:11]
	s_waitcnt vmcnt(3)
	v_cvt_pk_bf16_f32 v58, v58, v59
	v_cvt_pk_bf16_f32 v59, v60, v61
	v_cvt_pk_bf16_f32 v60, v62, v63
	v_cvt_pk_bf16_f32 v61, v64, v65
	global_store_dwordx4 v[4:5], v[58:61], off
	v_lshl_add_u64 v[4:5], v[4:5], 0, s[10:11]
	s_sub_u32 s4, s4, 1
	s_cmp_lg_u32 s4, 0
	s_cbranch_scc1 .Lpcvt_loop
	s_branch .LBB0_100

; __device__ __forceinline__ unsigned xb_ld(unsigned* p)              { return __hip_atomic_load(p, __ATOMIC_RELAXED, __HIP_MEMORY_SCOPE_AGENT); }
; __device__ __forceinline__ unsigned xb_add(unsigned* p, unsigned v) { return __hip_atomic_fetch_add(p, v, __ATOMIC_RELAXED, __HIP_MEMORY_SCOPE_AGENT); }
; #define XB_SPIN(cond, bar) do { unsigned _sp = 0; while (cond) { __builtin_amdgcn_s_sleep(1); \
;     if ((++_sp & 255u) == 0u) { if (xb_ld(&(bar)[XB_TMO])) break; if (_sp > XB_SPIN_CAP) { atomicAdd(&(bar)[XB_TMO], 1u); break; } } } } while (0)
; __device__ __forceinline__ void xcd_barrier(const XcdBarrier& b) {
;     ...
;         unsigned nloc = b.st[0], nx = b.st[1];
;         if (nloc == 0u) { xcd_barrier_complete(bar, b.x, nloc, nx); b.st[0] = nloc; b.st[1] = nx; }
;         const unsigned old = xb_add(&bar[XB_XSUB(b.x)], 1u);
;         const unsigned gen = old / nloc;
;         if (old + 1u == (gen + 1u) * nloc) {
;     ...
;             XB_SPIN(xb_ld(&bar[XB_XGEN(b.x)]) == gen, bar);
.LBB0_125:
	s_or_b64 exec, exec, s[8:9]
	v_cvt_f32_u32_e32 v5, v3
	s_waitcnt vmcnt(0)
	buffer_inv sc1
	v_readfirstlane_b32 s6, v4
	v_sub_u32_e32 v4, 0, v3
	v_rcp_iflag_f32_e32 v5, v5
	v_add_u32_e32 v6, s6, v2
	v_mul_f32_e32 v5, 0x4f7ffffe, v5
	v_cvt_u32_f32_e32 v5, v5
	v_mul_lo_u32 v2, v4, v5
	v_mul_hi_u32 v2, v5, v2
	v_add_u32_e32 v2, v5, v2
	v_mul_hi_u32 v2, v6, v2
	v_mul_lo_u32 v4, v2, v3
	v_sub_u32_e32 v4, v6, v4
	v_add_u32_e32 v5, 1, v2
	v_cmp_ge_u32_e32 vcc, v4, v3
	s_nop 1
	v_cndmask_b32_e32 v2, v2, v5, vcc
	v_sub_u32_e32 v5, v4, v3
	v_cndmask_b32_e32 v4, v4, v5, vcc
	v_add_u32_e32 v5, 1, v2
	v_cmp_ge_u32_e32 vcc, v4, v3
	v_add_u32_e32 v4, 1, v6
	s_nop 0
	v_cndmask_b32_e32 v2, v2, v5, vcc
	v_mul_lo_u32 v5, v3, v2
	v_add_u32_e32 v3, v5, v3
	v_cmp_ne_u32_e32 vcc, v4, v3
	s_and_saveexec_b64 s[6:7], vcc
	s_xor_b64 s[6:7], exec, s[6:7]
	s_cbranch_execz .LBB0_139
	s_waitcnt lgkmcnt(0)
	v_mov_b32_e32 v1, 0x2000
	global_load_dword v1, v1, s[4:5] offset:1024 sc1
	s_add_u32 s10, s4, 0x2400
	s_addc_u32 s11, s5, 0
	s_waitcnt vmcnt(0)
	v_cmp_eq_u32_e32 vcc, v1, v2
	s_and_saveexec_b64 s[8:9], vcc
	s_cbranch_execz .LBB0_138
	s_mov_b32 s22, 1
	s_mov_b64 s[12:13], 0
	v_mov_b32_e32 v1, 0
	s_branch .LBB0_129

; __device__ __forceinline__ unsigned xb_ld(unsigned* p)              { return __hip_atomic_load(p, __ATOMIC_RELAXED, __HIP_MEMORY_SCOPE_AGENT); }
; #define XB_SPIN(cond, bar) do { unsigned _sp = 0; while (cond) { __builtin_amdgcn_s_sleep(1); \
;     if ((++_sp & 255u) == 0u) { if (xb_ld(&(bar)[XB_TMO])) break; if (_sp > XB_SPIN_CAP) { atomicAdd(&(bar)[XB_TMO], 1u); break; } } } } while (0)
; __device__ __forceinline__ void xcd_barrier(const XcdBarrier& b) {
;     ...
;             XB_SPIN(xb_ld(&bar[XB_XGEN(b.x)]) == gen, bar);
;             __builtin_amdgcn_fence(__ATOMIC_ACQUIRE, "agent");
;             asm volatile("s_waitcnt vmcnt(0)" ::: "memory");
.LBB0_138:
	s_or_b64 exec, exec, s[8:9]
	s_waitcnt vmcnt(0)
	s_waitcnt vmcnt(0)

; __device__ __forceinline__ unsigned xb_ld(unsigned* p)              { return __hip_atomic_load(p, __ATOMIC_RELAXED, __HIP_MEMORY_SCOPE_AGENT); }
; __device__ __forceinline__ unsigned xb_add(unsigned* p, unsigned v) { return __hip_atomic_fetch_add(p, v, __ATOMIC_RELAXED, __HIP_MEMORY_SCOPE_AGENT); }
; #define XB_SPIN(cond, bar) do { unsigned _sp = 0; while (cond) { __builtin_amdgcn_s_sleep(1); \
;     if ((++_sp & 255u) == 0u) { if (xb_ld(&(bar)[XB_TMO])) break; if (_sp > XB_SPIN_CAP) { atomicAdd(&(bar)[XB_TMO], 1u); break; } } } } while (0)
; __device__ __forceinline__ void xcd_barrier(const XcdBarrier& b) {
;     ...
;             if (og + 1u == (tg + 1u) * nx) xb_add(&bar[XB_TOPGEN], 1u);
;             else XB_SPIN(xb_ld(&bar[XB_TOPGEN]) == tg, bar);
;             __builtin_amdgcn_fence(__ATOMIC_ACQUIRE, "agent");
;             xb_add(&bar[XB_XGEN(b.x)], 1u);
.LBB0_156:
	s_or_b64 exec, exec, s[6:7]
	s_mov_b64 s[6:7], exec
	v_mbcnt_lo_u32_b32 v1, s6, 0
	v_mbcnt_hi_u32_b32 v1, s7, v1
	v_cmp_eq_u32_e32 vcc, 0, v1
	s_waitcnt vmcnt(0)
	s_and_saveexec_b64 s[8:9], vcc
	s_cbranch_execz .LBB0_158
	s_bcnt1_i32_b64 s6, s[6:7]
	v_mov_b32_e32 v1, 0x2000
	v_mov_b32_e32 v2, s6
	global_atomic_add v1, v2, s[4:5] offset:1024

; __device__ __forceinline__ unsigned pk2(float lo, float hi) { unsigned r; asm("v_cvt_pk_bf16_f32 %0, %1, %2" : "=v"(r) : "v"(lo), "v"(hi)); return r; }
; template <int MODE>
; __device__ __forceinline__ void phase_rowpass1(const Ptrs& P, LAS unsigned char* lds, int layer, int tid_, int vcu, int G) {
;     ...
;         for (int idx = tid; idx < 4096; idx += NTHR) { const int k = idx >> 2, q = idx & 3; const f32x4 v = *(const f32x4*)(P.w_in + ((size_t)layer * 1024 + k) * DIN + 2304 + 4 * q);
;             gwt[(4 * q + 0) * 1024 + k] = (unsigned short)(pk2(v[0], 0.f) & 0xffffu); gwt[(4 * q + 1) * 1024 + k] = (unsigned short)(pk2(v[1], 0.f) & 0xffffu); gwt[(4 * q + 2) * 1024 + k] = (unsigned short)(pk2(v[2], 0.f) & 0xffffu); gwt[(4 * q + 3) * 1024 + k] = (unsigned short)(pk2(v[3], 0.f) & 0xffffu); }
.LBB0_261:
	s_waitcnt vmcnt(0)
	v_ashrrev_i32_e32 v10, 2, v5
	v_ashrrev_i32_e32 v11, 31, v10
	v_lshl_add_u64 v[6:7], s[20:21], 0, v[10:11]
	v_and_b32_e32 v12, 12, v4
	v_mad_u64_u32 v[8:9], s[4:5], v6, s63, v[2:3]
	v_lshlrev_b32_e32 v162, 2, v12
	v_mad_i32_i24 v9, v7, s63, v9
	v_lshl_add_u64 v[6:7], v[8:9], 0, v[162:163]
	v_add_co_u32_e32 v6, vcc, s62, v6
	s_nop 1
	v_addc_co_u32_e32 v7, vcc, 0, v7, vcc
	v_lshlrev_b32_e32 v12, 11, v12
	v_lshlrev_b32_e32 v10, 1, v10
	v_add3_u32 v10, 0, v12, v10
	s_mov_b32 s4, 0x122000
	s_mov_b32 s5, 0
	global_load_dwordx4 v[64:67], v[6:7], off offset:1024
	v_lshl_add_u64 v[6:7], v[6:7], 0, s[4:5]
	global_load_dwordx4 v[68:71], v[6:7], off offset:1024
	v_lshl_add_u64 v[6:7], v[6:7], 0, s[4:5]
	global_load_dwordx4 v[72:75], v[6:7], off offset:1024
	v_lshl_add_u64 v[6:7], v[6:7], 0, s[4:5]
	global_load_dwordx4 v[76:79], v[6:7], off offset:1024
	v_lshl_add_u64 v[6:7], v[6:7], 0, s[4:5]
	global_load_dwordx4 v[80:83], v[6:7], off offset:1024
	v_lshl_add_u64 v[6:7], v[6:7], 0, s[4:5]
	global_load_dwordx4 v[84:87], v[6:7], off offset:1024
	v_lshl_add_u64 v[6:7], v[6:7], 0, s[4:5]
	global_load_dwordx4 v[88:91], v[6:7], off offset:1024
	v_lshl_add_u64 v[6:7], v[6:7], 0, s[4:5]
	global_load_dwordx4 v[92:95], v[6:7], off offset:1024
	s_waitcnt vmcnt(7)
	v_cvt_pk_bf16_f32 v64, v64, v163
	v_cvt_pk_bf16_f32 v65, v65, v163
	v_cvt_pk_bf16_f32 v66, v66, v163
	v_cvt_pk_bf16_f32 v67, v67, v163
	ds_write_b16 v10, v64
	ds_write_b16 v10, v65 offset:2048
	ds_write_b16 v10, v66 offset:4096
	ds_write_b16 v10, v67 offset:6144
	s_waitcnt vmcnt(6)
	v_cvt_pk_bf16_f32 v68, v68, v163
	v_cvt_pk_bf16_f32 v69, v69, v163
	v_cvt_pk_bf16_f32 v70, v70, v163
	v_cvt_pk_bf16_f32 v71, v71, v163
	ds_write_b16 v10, v68 offset:256
	ds_write_b16 v10, v69 offset:2304
	ds_write_b16 v10, v70 offset:4352
	ds_write_b16 v10, v71 offset:6400
	s_waitcnt vmcnt(5)
	v_cvt_pk_bf16_f32 v72, v72, v163
	v_cvt_pk_bf16_f32 v73, v73, v163
	v_cvt_pk_bf16_f32 v74, v74, v163
	v_cvt_pk_bf16_f32 v75, v75, v163
	ds_write_b16 v10, v72 offset:512
	ds_write_b16 v10, v73 offset:2560
	ds_write_b16 v10, v74 offset:4608
	ds_write_b16 v10, v75 offset:6656
	s_waitcnt vmcnt(4)
	v_cvt_pk_bf16_f32 v76, v76, v163
	v_cvt_pk_bf16_f32 v77, v77, v163
	v_cvt_pk_bf16_f32 v78, v78, v163
	v_cvt_pk_bf16_f32 v79, v79, v163
	ds_write_b16 v10, v76 offset:768
	ds_write_b16 v10, v77 offset:2816
	ds_write_b16 v10, v78 offset:4864
	ds_write_b16 v10, v79 offset:6912
	s_waitcnt vmcnt(3)
	v_cvt_pk_bf16_f32 v80, v80, v163
	v_cvt_pk_bf16_f32 v81, v81, v163
	v_cvt_pk_bf16_f32 v82, v82, v163
	v_cvt_pk_bf16_f32 v83, v83, v163
	ds_write_b16 v10, v80 offset:1024
	ds_write_b16 v10, v81 offset:3072
	ds_write_b16 v10, v82 offset:5120
	ds_write_b16 v10, v83 offset:7168
	s_waitcnt vmcnt(2)
	v_cvt_pk_bf16_f32 v84, v84, v163
	v_cvt_pk_bf16_f32 v85, v85, v163
	v_cvt_pk_bf16_f32 v86, v86, v163
	v_cvt_pk_bf16_f32 v87, v87, v163
	ds_write_b16 v10, v84 offset:1280
	ds_write_b16 v10, v85 offset:3328
	ds_write_b16 v10, v86 offset:5376
	ds_write_b16 v10, v87 offset:7424
	s_waitcnt vmcnt(1)
	v_cvt_pk_bf16_f32 v88, v88, v163
	v_cvt_pk_bf16_f32 v89, v89, v163
	v_cvt_pk_bf16_f32 v90, v90, v163
	v_cvt_pk_bf16_f32 v91, v91, v163
	ds_write_b16 v10, v88 offset:1536
	ds_write_b16 v10, v89 offset:3584
	ds_write_b16 v10, v90 offset:5632
	ds_write_b16 v10, v91 offset:7680
	s_waitcnt vmcnt(0)
	v_cvt_pk_bf16_f32 v92, v92, v163
	v_cvt_pk_bf16_f32 v93, v93, v163
	v_cvt_pk_bf16_f32 v94, v94, v163
	v_cvt_pk_bf16_f32 v95, v95, v163
	ds_write_b16 v10, v92 offset:1792
	ds_write_b16 v10, v93 offset:3840
	ds_write_b16 v10, v94 offset:5888
	ds_write_b16 v10, v95 offset:7936

; __device__ __forceinline__ unsigned pk2(float lo, float hi) { unsigned r; asm("v_cvt_pk_bf16_f32 %0, %1, %2" : "=v"(r) : "v"(lo), "v"(hi)); return r; }
; template <int MODE>
; __device__ __forceinline__ void phase_rowpass1(const Ptrs& P, LAS unsigned char* lds, int layer, int tid_, int vcu, int G) {
;     ...
;         for (int idx = tid; idx < 4096; idx += NTHR) { const int k = idx >> 2, q = idx & 3; const f32x4 v = *(const f32x4*)(P.w_in + ((size_t)layer * 1024 + k) * DIN + 2304 + 4 * q);
;             gwt[(4 * q + 0) * 1024 + k] = (unsigned short)(pk2(v[0], 0.f) & 0xffffu); gwt[(4 * q + 1) * 1024 + k] = (unsigned short)(pk2(v[1], 0.f) & 0xffffu); gwt[(4 * q + 2) * 1024 + k] = (unsigned short)(pk2(v[2], 0.f) & 0xffffu); gwt[(4 * q + 3) * 1024 + k] = (unsigned short)(pk2(v[3], 0.f) & 0xffffu); }
.LBB0_274:
	s_waitcnt vmcnt(0)
	v_ashrrev_i32_e32 v8, 2, v3
	v_mov_b64_e32 v[4:5], s[66:67]
	v_and_b32_e32 v9, 12, v1
	v_mad_i64_i32 v[4:5], s[4:5], v8, s63, v[4:5]
	v_lshlrev_b32_e32 v162, 2, v9
	v_lshl_add_u64 v[4:5], v[4:5], 0, v[162:163]
	v_add_co_u32_e32 v4, vcc, 0x2000, v4
	s_nop 1
	v_addc_co_u32_e32 v5, vcc, 0, v5, vcc
	v_lshlrev_b32_e32 v9, 11, v9
	v_lshlrev_b32_e32 v8, 1, v8
	v_add3_u32 v8, 0, v9, v8
	s_mov_b32 s4, 0x122000
	s_mov_b32 s5, 0
	global_load_dwordx4 v[64:67], v[4:5], off offset:1024
	v_lshl_add_u64 v[4:5], v[4:5], 0, s[4:5]
	global_load_dwordx4 v[68:71], v[4:5], off offset:1024
	v_lshl_add_u64 v[4:5], v[4:5], 0, s[4:5]
	global_load_dwordx4 v[72:75], v[4:5], off offset:1024
	v_lshl_add_u64 v[4:5], v[4:5], 0, s[4:5]
	global_load_dwordx4 v[76:79], v[4:5], off offset:1024
	v_lshl_add_u64 v[4:5], v[4:5], 0, s[4:5]
	global_load_dwordx4 v[80:83], v[4:5], off offset:1024
	v_lshl_add_u64 v[4:5], v[4:5], 0, s[4:5]
	global_load_dwordx4 v[84:87], v[4:5], off offset:1024
	v_lshl_add_u64 v[4:5], v[4:5], 0, s[4:5]
	global_load_dwordx4 v[88:91], v[4:5], off offset:1024
	v_lshl_add_u64 v[4:5], v[4:5], 0, s[4:5]
	global_load_dwordx4 v[92:95], v[4:5], off offset:1024
	s_waitcnt vmcnt(7)
	v_cvt_pk_bf16_f32 v64, v64, v163
	v_cvt_pk_bf16_f32 v65, v65, v163
	v_cvt_pk_bf16_f32 v66, v66, v163
	v_cvt_pk_bf16_f32 v67, v67, v163
	ds_write_b16 v8, v64
	ds_write_b16 v8, v65 offset:2048
	ds_write_b16 v8, v66 offset:4096
	ds_write_b16 v8, v67 offset:6144
	s_waitcnt vmcnt(6)
	v_cvt_pk_bf16_f32 v68, v68, v163
	v_cvt_pk_bf16_f32 v69, v69, v163
	v_cvt_pk_bf16_f32 v70, v70, v163
	v_cvt_pk_bf16_f32 v71, v71, v163
	ds_write_b16 v8, v68 offset:256
	ds_write_b16 v8, v69 offset:2304
	ds_write_b16 v8, v70 offset:4352
	ds_write_b16 v8, v71 offset:6400
	s_waitcnt vmcnt(5)
	v_cvt_pk_bf16_f32 v72, v72, v163
	v_cvt_pk_bf16_f32 v73, v73, v163
	v_cvt_pk_bf16_f32 v74, v74, v163
	v_cvt_pk_bf16_f32 v75, v75, v163
	ds_write_b16 v8, v72 offset:512
	ds_write_b16 v8, v73 offset:2560
	ds_write_b16 v8, v74 offset:4608
	ds_write_b16 v8, v75 offset:6656
	s_waitcnt vmcnt(4)
	v_cvt_pk_bf16_f32 v76, v76, v163
	v_cvt_pk_bf16_f32 v77, v77, v163
	v_cvt_pk_bf16_f32 v78, v78, v163
	v_cvt_pk_bf16_f32 v79, v79, v163
	ds_write_b16 v8, v76 offset:768
	ds_write_b16 v8, v77 offset:2816
	ds_write_b16 v8, v78 offset:4864
	ds_write_b16 v8, v79 offset:6912
	s_waitcnt vmcnt(3)
	v_cvt_pk_bf16_f32 v80, v80, v163
	v_cvt_pk_bf16_f32 v81, v81, v163
	v_cvt_pk_bf16_f32 v82, v82, v163
	v_cvt_pk_bf16_f32 v83, v83, v163
	ds_write_b16 v8, v80 offset:1024
	ds_write_b16 v8, v81 offset:3072
	ds_write_b16 v8, v82 offset:5120
	ds_write_b16 v8, v83 offset:7168
	s_waitcnt vmcnt(2)
	v_cvt_pk_bf16_f32 v84, v84, v163
	v_cvt_pk_bf16_f32 v85, v85, v163
	v_cvt_pk_bf16_f32 v86, v86, v163
	v_cvt_pk_bf16_f32 v87, v87, v163
	ds_write_b16 v8, v84 offset:1280
	ds_write_b16 v8, v85 offset:3328
	ds_write_b16 v8, v86 offset:5376
	ds_write_b16 v8, v87 offset:7424
	s_waitcnt vmcnt(1)
	v_cvt_pk_bf16_f32 v88, v88, v163
	v_cvt_pk_bf16_f32 v89, v89, v163
	v_cvt_pk_bf16_f32 v90, v90, v163
	v_cvt_pk_bf16_f32 v91, v91, v163
	ds_write_b16 v8, v88 offset:1536
	ds_write_b16 v8, v89 offset:3584
	ds_write_b16 v8, v90 offset:5632
	ds_write_b16 v8, v91 offset:7680
	s_waitcnt vmcnt(0)
	v_cvt_pk_bf16_f32 v92, v92, v163
	v_cvt_pk_bf16_f32 v93, v93, v163
	v_cvt_pk_bf16_f32 v94, v94, v163
	v_cvt_pk_bf16_f32 v95, v95, v163
	ds_write_b16 v8, v92 offset:1792
	ds_write_b16 v8, v93 offset:3840
	ds_write_b16 v8, v94 offset:5888
	ds_write_b16 v8, v95 offset:7936

; __device__ __forceinline__ unsigned xb_ld(unsigned* p)              { return __hip_atomic_load(p, __ATOMIC_RELAXED, __HIP_MEMORY_SCOPE_AGENT); }
; __device__ __forceinline__ unsigned xb_add(unsigned* p, unsigned v) { return __hip_atomic_fetch_add(p, v, __ATOMIC_RELAXED, __HIP_MEMORY_SCOPE_AGENT); }
; #define XB_SPIN(cond, bar) do { unsigned _sp = 0; while (cond) { __builtin_amdgcn_s_sleep(1); \
;     if ((++_sp & 255u) == 0u) { if (xb_ld(&(bar)[XB_TMO])) break; if (_sp > XB_SPIN_CAP) { atomicAdd(&(bar)[XB_TMO], 1u); break; } } } } while (0)
; __device__ __forceinline__ void xcd_barrier(const XcdBarrier& b) {
;     ...
;         unsigned nloc = b.st[0], nx = b.st[1];
;         if (nloc == 0u) { xcd_barrier_complete(bar, b.x, nloc, nx); b.st[0] = nloc; b.st[1] = nx; }
;         const unsigned old = xb_add(&bar[XB_XSUB(b.x)], 1u);
;         const unsigned gen = old / nloc;
;         if (old + 1u == (gen + 1u) * nloc) {
;     ...
;             XB_SPIN(xb_ld(&bar[XB_XGEN(b.x)]) == gen, bar);
.LBB0_301:
	s_or_b64 exec, exec, s[6:7]
	v_cvt_f32_u32_e32 v5, v3
	s_waitcnt vmcnt(0)
	buffer_inv sc1
	v_readfirstlane_b32 s5, v4
	v_sub_u32_e32 v4, 0, v3
	v_rcp_iflag_f32_e32 v5, v5
	v_add_u32_e32 v6, s5, v1
	v_mul_f32_e32 v5, 0x4f7ffffe, v5
	v_cvt_u32_f32_e32 v5, v5
	v_mul_lo_u32 v1, v4, v5
	v_mul_hi_u32 v1, v5, v1
	v_add_u32_e32 v1, v5, v1
	v_mul_hi_u32 v1, v6, v1
	v_mul_lo_u32 v4, v1, v3
	v_sub_u32_e32 v4, v6, v4
	v_add_u32_e32 v5, 1, v1
	v_cmp_ge_u32_e32 vcc, v4, v3
	s_nop 1
	v_cndmask_b32_e32 v1, v1, v5, vcc
	v_sub_u32_e32 v5, v4, v3
	v_cndmask_b32_e32 v4, v4, v5, vcc
	v_add_u32_e32 v5, 1, v1
	v_cmp_ge_u32_e32 vcc, v4, v3
	v_add_u32_e32 v4, 1, v6
	s_nop 0
	v_cndmask_b32_e32 v1, v1, v5, vcc
	v_mul_lo_u32 v5, v3, v1
	v_add_u32_e32 v3, v5, v3
	v_cmp_ne_u32_e32 vcc, v4, v3
	s_and_saveexec_b64 s[6:7], vcc
	s_xor_b64 s[6:7], exec, s[6:7]
	s_cbranch_execz .LBB0_315
	v_readlane_b32 s8, v253, 48
	v_readlane_b32 s9, v253, 49
	s_waitcnt lgkmcnt(0)
	s_nop 3
	global_load_dword v2, v163, s[8:9] sc1
	s_waitcnt vmcnt(0)
	v_cmp_eq_u32_e32 vcc, v2, v1
	s_and_saveexec_b64 s[8:9], vcc
	s_cbranch_execz .LBB0_314
	s_mov_b32 s5, 1
	s_mov_b64 s[12:13], 0
	s_branch .LBB0_305

; __device__ __forceinline__ unsigned xb_ld(unsigned* p)              { return __hip_atomic_load(p, __ATOMIC_RELAXED, __HIP_MEMORY_SCOPE_AGENT); }
; __device__ __forceinline__ unsigned xb_add(unsigned* p, unsigned v) { return __hip_atomic_fetch_add(p, v, __ATOMIC_RELAXED, __HIP_MEMORY_SCOPE_AGENT); }
; #define XB_SPIN(cond, bar) do { unsigned _sp = 0; while (cond) { __builtin_amdgcn_s_sleep(1); \
;     if ((++_sp & 255u) == 0u) { if (xb_ld(&(bar)[XB_TMO])) break; if (_sp > XB_SPIN_CAP) { atomicAdd(&(bar)[XB_TMO], 1u); break; } } } } while (0)
; __device__ __forceinline__ void xcd_barrier(const XcdBarrier& b) {
;     ...
;             if (og + 1u == (tg + 1u) * nx) xb_add(&bar[XB_TOPGEN], 1u);
;             else XB_SPIN(xb_ld(&bar[XB_TOPGEN]) == tg, bar);
;             __builtin_amdgcn_fence(__ATOMIC_ACQUIRE, "agent");
;             xb_add(&bar[XB_XGEN(b.x)], 1u);
.LBB0_332:
	s_or_b64 exec, exec, s[6:7]
	s_mov_b64 s[6:7], exec
	v_mbcnt_lo_u32_b32 v1, s6, 0
	v_mbcnt_hi_u32_b32 v1, s7, v1
	v_cmp_eq_u32_e32 vcc, 0, v1
	s_waitcnt vmcnt(0)
	s_and_saveexec_b64 s[8:9], vcc
	s_cbranch_execz .LBB0_334
	s_bcnt1_i32_b64 s5, s[6:7]
	v_readlane_b32 s6, v253, 48
	v_mov_b32_e32 v1, s5
	v_readlane_b32 s7, v253, 49
	s_nop 4
	global_atomic_add v163, v1, s[6:7]

; __device__ __forceinline__ unsigned xb_ld(unsigned* p)              { return __hip_atomic_load(p, __ATOMIC_RELAXED, __HIP_MEMORY_SCOPE_AGENT); }
; __device__ __forceinline__ unsigned xb_add(unsigned* p, unsigned v) { return __hip_atomic_fetch_add(p, v, __ATOMIC_RELAXED, __HIP_MEMORY_SCOPE_AGENT); }
; #define XB_SPIN(cond, bar) do { unsigned _sp = 0; while (cond) { __builtin_amdgcn_s_sleep(1); \
;     if ((++_sp & 255u) == 0u) { if (xb_ld(&(bar)[XB_TMO])) break; if (_sp > XB_SPIN_CAP) { atomicAdd(&(bar)[XB_TMO], 1u); break; } } } } while (0)
; __device__ __forceinline__ void xcd_barrier(const XcdBarrier& b) {
;     ...
;         unsigned nloc = b.st[0], nx = b.st[1];
;         if (nloc == 0u) { xcd_barrier_complete(bar, b.x, nloc, nx); b.st[0] = nloc; b.st[1] = nx; }
;         const unsigned old = xb_add(&bar[XB_XSUB(b.x)], 1u);
;         const unsigned gen = old / nloc;
;         if (old + 1u == (gen + 1u) * nloc) {
;     ...
;             XB_SPIN(xb_ld(&bar[XB_XGEN(b.x)]) == gen, bar);
.LBB0_1538:
	s_or_b64 exec, exec, s[6:7]
	v_cvt_f32_u32_e32 v5, v3
	s_waitcnt vmcnt(0)
	buffer_inv sc1
	v_readfirstlane_b32 s4, v4
	v_sub_u32_e32 v4, 0, v3
	v_rcp_iflag_f32_e32 v5, v5
	v_add_u32_e32 v6, s4, v1
	v_mul_f32_e32 v5, 0x4f7ffffe, v5
	v_cvt_u32_f32_e32 v5, v5
	v_mul_lo_u32 v1, v4, v5
	v_mul_hi_u32 v1, v5, v1
	v_add_u32_e32 v1, v5, v1
	v_mul_hi_u32 v1, v6, v1
	v_mul_lo_u32 v4, v1, v3
	v_sub_u32_e32 v4, v6, v4
	v_add_u32_e32 v5, 1, v1
	v_cmp_ge_u32_e32 vcc, v4, v3
	s_nop 1
	v_cndmask_b32_e32 v1, v1, v5, vcc
	v_sub_u32_e32 v5, v4, v3
	v_cndmask_b32_e32 v4, v4, v5, vcc
	v_add_u32_e32 v5, 1, v1
	v_cmp_ge_u32_e32 vcc, v4, v3
	v_add_u32_e32 v4, 1, v6
	s_nop 0
	v_cndmask_b32_e32 v1, v1, v5, vcc
	v_mul_lo_u32 v5, v3, v1
	v_add_u32_e32 v3, v5, v3
	v_cmp_ne_u32_e32 vcc, v4, v3
	s_and_saveexec_b64 s[4:5], vcc
	s_xor_b64 s[6:7], exec, s[4:5]
	s_cbranch_execz .LBB0_1552
	v_readlane_b32 s4, v253, 48
	v_readlane_b32 s5, v253, 49
	s_waitcnt lgkmcnt(0)
	s_nop 3
	global_load_dword v2, v163, s[4:5] sc1
	s_waitcnt vmcnt(0)
	v_cmp_eq_u32_e32 vcc, v2, v1
	s_and_saveexec_b64 s[8:9], vcc
	s_cbranch_execz .LBB0_1551
	s_mov_b32 s4, 1
	s_mov_b64 s[12:13], 0
	s_branch .LBB0_1542

; __device__ __forceinline__ unsigned xb_ld(unsigned* p)              { return __hip_atomic_load(p, __ATOMIC_RELAXED, __HIP_MEMORY_SCOPE_AGENT); }
; __device__ __forceinline__ unsigned xb_add(unsigned* p, unsigned v) { return __hip_atomic_fetch_add(p, v, __ATOMIC_RELAXED, __HIP_MEMORY_SCOPE_AGENT); }
; #define XB_SPIN(cond, bar) do { unsigned _sp = 0; while (cond) { __builtin_amdgcn_s_sleep(1); \
;     if ((++_sp & 255u) == 0u) { if (xb_ld(&(bar)[XB_TMO])) break; if (_sp > XB_SPIN_CAP) { atomicAdd(&(bar)[XB_TMO], 1u); break; } } } } while (0)
; __device__ __forceinline__ void xcd_barrier(const XcdBarrier& b) {
;     ...
;             if (og + 1u == (tg + 1u) * nx) xb_add(&bar[XB_TOPGEN], 1u);
;             else XB_SPIN(xb_ld(&bar[XB_TOPGEN]) == tg, bar);
;             __builtin_amdgcn_fence(__ATOMIC_ACQUIRE, "agent");
;             xb_add(&bar[XB_XGEN(b.x)], 1u);
.LBB0_1569:
	s_or_b64 exec, exec, s[6:7]
	s_mov_b64 s[6:7], exec
	v_mbcnt_lo_u32_b32 v1, s6, 0
	v_mbcnt_hi_u32_b32 v1, s7, v1
	v_cmp_eq_u32_e32 vcc, 0, v1
	s_waitcnt vmcnt(0)
	s_and_saveexec_b64 s[8:9], vcc
	s_cbranch_execnz .LBB0_1570
	s_getpc_b64 s[98:99]
